# pipelined attention: no softmax VALU in the first 8 MFMAs after each barrier
# speedup vs baseline: 1.0141x; 1.0081x over previous
.LBB0_734:
	s_waitcnt lgkmcnt(0)
	s_barrier
	ds_read_b128 v[160:163], v201 offset:16384
	ds_read_b128 v[164:167], v209 offset:0
	ds_read_b128 v[168:171], v202 offset:16384
	ds_read_b128 v[172:175], v209 offset:2048
	ds_read_b128 v[176:179], v203 offset:16384
	ds_read_b128 v[180:183], v209 offset:4096
	ds_read_b128 v[230:233], v246 offset:16384
	s_waitcnt lgkmcnt(6)
	v_mfma_f32_16x16x32_bf16 v[64:67], v[160:163], v[96:99], 0
	v_mfma_f32_16x16x32_bf16 v[68:71], v[160:163], v[112:115], 0
	ds_read_b128 v[234:237], v209 offset:6144
	s_add_u32 s16, s22, s10
	s_addc_u32 s17, s23, s11
	s_add_u32 s15, s22, s12
	s_addc_u32 s14, s23, s13
	s_add_u32 s8, s16, 0x3bc00200
	s_addc_u32 s9, s17, 0
	s_add_u32 s6, s15, 0x23a50000
	s_addc_u32 s7, s14, 0
	s_waitcnt lgkmcnt(6)
	v_mfma_f32_16x16x32_bf16 v[0:3], v[164:167], v[216:219], v[0:3]
	v_mfma_f32_16x16x32_bf16 v[4:7], v[164:167], v[238:241], v[4:7]
	ds_read_b128 v[160:163], v201 offset:20480
	s_waitcnt vmcnt(4)
	ds_write_b128 v225, v[152:155] offset:49152
	s_waitcnt lgkmcnt(7)
	v_mfma_f32_16x16x32_bf16 v[68:71], v[168:171], v[116:119], v[68:71]
	v_mfma_f32_16x16x32_bf16 v[64:67], v[168:171], v[100:103], v[64:67]
	ds_read_b128 v[164:167], v209 offset:8192
	ds_write_b128 v226, v[156:159] offset:49152
	s_waitcnt lgkmcnt(8)
	v_mfma_f32_16x16x32_bf16 v[12:15], v[172:175], v[238:241], v[12:15]
	v_mfma_f32_16x16x32_bf16 v[8:11], v[172:175], v[216:219], v[8:11]
	ds_read_b128 v[168:171], v202 offset:20480
	ds_write_b64 v227, v[132:133] offset:32768
	s_waitcnt lgkmcnt(9)
	v_mfma_f32_16x16x32_bf16 v[64:67], v[176:179], v[104:107], v[64:67]
	v_exp_f32_e32 v88, v88
	v_exp_f32_e32 v92, v92
	v_mfma_f32_16x16x32_bf16 v[68:71], v[176:179], v[120:123], v[68:71]
	v_cvt_pk_bf16_f32 v242, v80, v81
	v_exp_f32_e32 v89, v89
	ds_read_b128 v[172:175], v209 offset:10240
	ds_write_b64 v228, v[134:135] offset:32768
	s_waitcnt lgkmcnt(10)
	v_mfma_f32_16x16x32_bf16 v[16:19], v[180:183], v[216:219], v[16:19]
	v_exp_f32_e32 v93, v93
	v_cvt_pk_bf16_f32 v243, v82, v83
	v_mfma_f32_16x16x32_bf16 v[20:23], v[180:183], v[238:241], v[20:23]
	v_exp_f32_e32 v90, v90
	v_exp_f32_e32 v94, v94
	ds_read_b128 v[176:179], v203 offset:20480
	ds_write_b64 v229, v[128:129] offset:32768
	s_waitcnt lgkmcnt(11)
	v_mfma_f32_16x16x32_bf16 v[68:71], v[230:233], v[124:127], v[68:71]
	v_cvt_pk_bf16_f32 v204, v84, v85
	v_exp_f32_e32 v91, v91
	v_mfma_f32_16x16x32_bf16 v[64:67], v[230:233], v[108:111], v[64:67]
	v_exp_f32_e32 v95, v95
	v_cvt_pk_bf16_f32 v205, v86, v87
	ds_read_b128 v[180:183], v209 offset:12288
	ds_write_b64 v184, v[130:131] offset:32768
	s_waitcnt lgkmcnt(12)
	v_mfma_f32_16x16x32_bf16 v[28:31], v[234:237], v[238:241], v[28:31]
	v_add_f32_e32 v220, v220, v88
	v_add_f32_e32 v221, v221, v92
	v_mfma_f32_16x16x32_bf16 v[24:27], v[234:237], v[216:219], v[24:27]
	v_add_f32_e32 v220, v220, v89
	v_add_f32_e32 v221, v221, v93
	ds_read_b128 v[230:233], v246 offset:20480
	global_load_dwordx4 v[132:135], v198, s[8:9]
	s_waitcnt lgkmcnt(12)
	v_mfma_f32_16x16x32_bf16 v[72:75], v[160:163], v[96:99], 0
	v_cvt_pk_bf16_f32 v244, v88, v89
	v_cvt_pk_bf16_f32 v245, v90, v91
	v_mfma_f32_16x16x32_bf16 v[76:79], v[160:163], v[112:115], 0
	v_cvt_pk_bf16_f32 v206, v92, v93
	v_cvt_pk_bf16_f32 v207, v94, v95
	ds_read_b128 v[234:237], v209 offset:14336
	global_load_dwordx4 v[128:131], v199, s[8:9]
	s_waitcnt lgkmcnt(11)
	v_mfma_f32_16x16x32_bf16 v[32:35], v[164:167], v[216:219], v[32:35]
	v_add_f32_e32 v220, v220, v90
	v_add_f32_e32 v221, v221, v94
	v_mfma_f32_16x16x32_bf16 v[36:39], v[164:167], v[238:241], v[36:39]
	v_add_f32_e32 v220, v220, v91
	v_add_f32_e32 v221, v221, v95
	ds_read_b128 v[160:163], v201 offset:24576
	global_load_dwordx4 v[152:155], v196, s[6:7]
	s_waitcnt lgkmcnt(10)
	v_mfma_f32_16x16x32_bf16 v[76:79], v[168:171], v[116:119], v[76:79]
	v_add_f32_e32 v194, v194, v220
	v_add_f32_e32 v195, v195, v221
	v_mfma_f32_16x16x32_bf16 v[72:75], v[168:171], v[100:103], v[72:75]
	v_exp_f32_e32 v64, v64
	v_exp_f32_e32 v68, v68
	ds_read_b128 v[164:167], v210 offset:0
	global_load_dwordx4 v[156:159], v197, s[6:7]
	s_waitcnt lgkmcnt(9)
	v_mfma_f32_16x16x32_bf16 v[44:47], v[172:175], v[238:241], v[44:47]
	v_exp_f32_e32 v65, v65
	v_exp_f32_e32 v69, v69
	v_mfma_f32_16x16x32_bf16 v[40:43], v[172:175], v[216:219], v[40:43]
	v_exp_f32_e32 v66, v66
	v_exp_f32_e32 v70, v70
	ds_read_b128 v[168:171], v202 offset:24576
	s_waitcnt lgkmcnt(8)
	v_mfma_f32_16x16x32_bf16 v[72:75], v[176:179], v[104:107], v[72:75]
	v_exp_f32_e32 v67, v67
	v_mfma_f32_16x16x32_bf16 v[76:79], v[176:179], v[120:123], v[76:79]
	v_exp_f32_e32 v71, v71
	ds_read_b128 v[172:175], v210 offset:2048
	s_waitcnt lgkmcnt(7)
	v_mfma_f32_16x16x32_bf16 v[48:51], v[180:183], v[216:219], v[48:51]
	v_add_f32_e32 v220, v64, v65
	v_mfma_f32_16x16x32_bf16 v[52:55], v[180:183], v[238:241], v[52:55]
	v_add_f32_e32 v221, v68, v69
	ds_read_b128 v[176:179], v203 offset:24576
	s_waitcnt lgkmcnt(6)
	v_mfma_f32_16x16x32_bf16 v[76:79], v[230:233], v[124:127], v[76:79]
	v_add_f32_e32 v220, v220, v66
	v_mfma_f32_16x16x32_bf16 v[72:75], v[230:233], v[108:111], v[72:75]
	v_add_f32_e32 v221, v221, v70
	ds_read_b128 v[180:183], v210 offset:4096
	s_waitcnt lgkmcnt(6)
	v_mfma_f32_16x16x32_bf16 v[60:63], v[234:237], v[238:241], v[60:63]
	v_add_f32_e32 v220, v220, v67
	v_mfma_f32_16x16x32_bf16 v[56:59], v[234:237], v[216:219], v[56:59]
	v_add_f32_e32 v221, v221, v71
	ds_read_b128 v[230:233], v246 offset:24576
	s_waitcnt lgkmcnt(6)
	v_mfma_f32_16x16x32_bf16 v[80:83], v[160:163], v[96:99], 0
	v_exp_f32_e32 v72, v72
	v_exp_f32_e32 v76, v76
	v_mfma_f32_16x16x32_bf16 v[84:87], v[160:163], v[112:115], 0
	v_exp_f32_e32 v73, v73
	v_exp_f32_e32 v77, v77
	ds_read_b128 v[234:237], v210 offset:6144
	s_waitcnt lgkmcnt(6)
	v_mfma_f32_16x16x32_bf16 v[0:3], v[164:167], v[242:245], v[0:3]
	v_exp_f32_e32 v74, v74
	v_exp_f32_e32 v78, v78
	v_mfma_f32_16x16x32_bf16 v[4:7], v[164:167], v[204:207], v[4:7]
	v_exp_f32_e32 v75, v75
	v_exp_f32_e32 v79, v79
	ds_read_b128 v[160:163], v201 offset:28672
	s_waitcnt lgkmcnt(6)
	v_mfma_f32_16x16x32_bf16 v[84:87], v[168:171], v[116:119], v[84:87]
	v_add_f32_e32 v220, v220, v72
	v_mfma_f32_16x16x32_bf16 v[80:83], v[168:171], v[100:103], v[80:83]
	v_add_f32_e32 v221, v221, v76
	ds_read_b128 v[164:167], v210 offset:8192
	s_waitcnt lgkmcnt(6)
	v_mfma_f32_16x16x32_bf16 v[12:15], v[172:175], v[204:207], v[12:15]
	v_add_f32_e32 v220, v220, v73
	v_mfma_f32_16x16x32_bf16 v[8:11], v[172:175], v[242:245], v[8:11]
	v_add_f32_e32 v221, v221, v77
	ds_read_b128 v[168:171], v202 offset:28672
	s_waitcnt lgkmcnt(6)
	v_mfma_f32_16x16x32_bf16 v[80:83], v[176:179], v[104:107], v[80:83]
	v_add_f32_e32 v220, v220, v74
	v_mfma_f32_16x16x32_bf16 v[84:87], v[176:179], v[120:123], v[84:87]
	v_add_f32_e32 v221, v221, v78
	ds_read_b128 v[172:175], v210 offset:10240
	s_waitcnt lgkmcnt(6)
	v_mfma_f32_16x16x32_bf16 v[16:19], v[180:183], v[242:245], v[16:19]
	v_add_f32_e32 v220, v220, v75
	v_mfma_f32_16x16x32_bf16 v[20:23], v[180:183], v[204:207], v[20:23]
	v_add_f32_e32 v221, v221, v79
	ds_read_b128 v[176:179], v203 offset:28672
	s_waitcnt lgkmcnt(6)
	v_mfma_f32_16x16x32_bf16 v[84:87], v[230:233], v[124:127], v[84:87]
	v_cvt_pk_bf16_f32 v216, v64, v65
	v_mfma_f32_16x16x32_bf16 v[80:83], v[230:233], v[108:111], v[80:83]
	v_cvt_pk_bf16_f32 v217, v66, v67
	ds_read_b128 v[180:183], v210 offset:12288
	s_waitcnt lgkmcnt(6)
	v_mfma_f32_16x16x32_bf16 v[28:31], v[234:237], v[204:207], v[28:31]
	v_cvt_pk_bf16_f32 v238, v68, v69
	v_mfma_f32_16x16x32_bf16 v[24:27], v[234:237], v[242:245], v[24:27]
	v_cvt_pk_bf16_f32 v239, v70, v71
	ds_read_b128 v[230:233], v246 offset:28672
	s_waitcnt lgkmcnt(6)
	v_mfma_f32_16x16x32_bf16 v[88:91], v[160:163], v[96:99], 0
	v_exp_f32_e32 v80, v80
	v_exp_f32_e32 v84, v84
	v_mfma_f32_16x16x32_bf16 v[92:95], v[160:163], v[112:115], 0
	v_exp_f32_e32 v81, v81
	v_exp_f32_e32 v85, v85
	ds_read_b128 v[234:237], v210 offset:14336
	s_waitcnt lgkmcnt(6)
	v_mfma_f32_16x16x32_bf16 v[32:35], v[164:167], v[242:245], v[32:35]
	v_exp_f32_e32 v82, v82
	v_exp_f32_e32 v86, v86
	v_mfma_f32_16x16x32_bf16 v[36:39], v[164:167], v[204:207], v[36:39]
	v_exp_f32_e32 v83, v83
	v_exp_f32_e32 v87, v87
	ds_read_b128 v[160:163], v201 offset:32768
	s_waitcnt lgkmcnt(6)
	v_mfma_f32_16x16x32_bf16 v[92:95], v[168:171], v[116:119], v[92:95]
	v_add_f32_e32 v220, v220, v80
	v_mfma_f32_16x16x32_bf16 v[88:91], v[168:171], v[100:103], v[88:91]
	v_add_f32_e32 v221, v221, v84
	ds_read_b128 v[164:167], v209 offset:16384
	s_waitcnt lgkmcnt(6)
	v_mfma_f32_16x16x32_bf16 v[44:47], v[172:175], v[204:207], v[44:47]
	v_add_f32_e32 v220, v220, v81
	v_mfma_f32_16x16x32_bf16 v[40:43], v[172:175], v[242:245], v[40:43]
	v_add_f32_e32 v221, v221, v85
	ds_read_b128 v[168:171], v202 offset:32768
	s_waitcnt lgkmcnt(6)
	v_mfma_f32_16x16x32_bf16 v[88:91], v[176:179], v[104:107], v[88:91]
	v_add_f32_e32 v220, v220, v82
	v_mfma_f32_16x16x32_bf16 v[92:95], v[176:179], v[120:123], v[92:95]
	v_add_f32_e32 v221, v221, v86
	ds_read_b128 v[172:175], v209 offset:18432
	s_waitcnt lgkmcnt(6)
	v_mfma_f32_16x16x32_bf16 v[48:51], v[180:183], v[242:245], v[48:51]
	v_add_f32_e32 v220, v220, v83
	v_mfma_f32_16x16x32_bf16 v[52:55], v[180:183], v[204:207], v[52:55]
	v_add_f32_e32 v221, v221, v87
	ds_read_b128 v[176:179], v203 offset:32768
	s_waitcnt lgkmcnt(6)
	v_mfma_f32_16x16x32_bf16 v[92:95], v[230:233], v[124:127], v[92:95]
	v_cvt_pk_bf16_f32 v218, v72, v73
	v_mfma_f32_16x16x32_bf16 v[88:91], v[230:233], v[108:111], v[88:91]
	v_cvt_pk_bf16_f32 v219, v74, v75
	ds_read_b128 v[180:183], v209 offset:20480
	s_waitcnt lgkmcnt(6)
	v_mfma_f32_16x16x32_bf16 v[60:63], v[234:237], v[204:207], v[60:63]
	v_cvt_pk_bf16_f32 v240, v76, v77
	v_mfma_f32_16x16x32_bf16 v[56:59], v[234:237], v[242:245], v[56:59]
	v_cvt_pk_bf16_f32 v241, v78, v79
	ds_read_b128 v[230:233], v246 offset:32768
	s_waitcnt lgkmcnt(6)
	v_mfma_f32_16x16x32_bf16 v[64:67], v[160:163], v[96:99], 0
	v_exp_f32_e32 v88, v88
	v_exp_f32_e32 v92, v92
	v_mfma_f32_16x16x32_bf16 v[68:71], v[160:163], v[112:115], 0
	v_cvt_pk_bf16_f32 v242, v80, v81
	v_exp_f32_e32 v89, v89
	ds_read_b128 v[234:237], v209 offset:22528
	s_add_u32 s8, s16, 0x3bc00280
	s_addc_u32 s9, s17, 0
	s_add_u32 s6, s15, 0x23a60000
	s_addc_u32 s7, s14, 0
	s_waitcnt lgkmcnt(6)
	v_mfma_f32_16x16x32_bf16 v[0:3], v[164:167], v[216:219], v[0:3]
	v_exp_f32_e32 v93, v93
	v_cvt_pk_bf16_f32 v243, v82, v83
	v_mfma_f32_16x16x32_bf16 v[4:7], v[164:167], v[238:241], v[4:7]
	v_exp_f32_e32 v90, v90
	v_exp_f32_e32 v94, v94
	ds_read_b128 v[160:163], v201 offset:36864
	s_waitcnt vmcnt(4)
	ds_write_b128 v225, v[136:139] offset:0
	s_waitcnt lgkmcnt(7)
	v_mfma_f32_16x16x32_bf16 v[68:71], v[168:171], v[116:119], v[68:71]
	v_cvt_pk_bf16_f32 v204, v84, v85
	v_mfma_f32_16x16x32_bf16 v[64:67], v[168:171], v[100:103], v[64:67]
	v_exp_f32_e32 v91, v91
	ds_read_b128 v[164:167], v209 offset:24576
	ds_write_b128 v226, v[140:143] offset:0
	s_waitcnt lgkmcnt(8)
	v_mfma_f32_16x16x32_bf16 v[12:15], v[172:175], v[238:241], v[12:15]
	v_exp_f32_e32 v95, v95
	v_mfma_f32_16x16x32_bf16 v[8:11], v[172:175], v[216:219], v[8:11]
	v_cvt_pk_bf16_f32 v205, v86, v87
	ds_read_b128 v[168:171], v202 offset:36864
	ds_write_b64 v227, v[148:149] offset:49152
	s_waitcnt lgkmcnt(9)
	v_mfma_f32_16x16x32_bf16 v[64:67], v[176:179], v[104:107], v[64:67]
	v_add_f32_e32 v220, v220, v88
	v_mfma_f32_16x16x32_bf16 v[68:71], v[176:179], v[120:123], v[68:71]
	v_add_f32_e32 v221, v221, v92
	ds_read_b128 v[172:175], v209 offset:26624
	ds_write_b64 v228, v[150:151] offset:49152
	s_waitcnt lgkmcnt(10)
	v_mfma_f32_16x16x32_bf16 v[16:19], v[180:183], v[216:219], v[16:19]
	v_add_f32_e32 v220, v220, v89
	v_mfma_f32_16x16x32_bf16 v[20:23], v[180:183], v[238:241], v[20:23]
	v_add_f32_e32 v221, v221, v93
	ds_read_b128 v[176:179], v203 offset:36864
	ds_write_b64 v229, v[144:145] offset:49152
	s_waitcnt lgkmcnt(11)
	v_mfma_f32_16x16x32_bf16 v[68:71], v[230:233], v[124:127], v[68:71]
	v_cvt_pk_bf16_f32 v244, v88, v89
	v_mfma_f32_16x16x32_bf16 v[64:67], v[230:233], v[108:111], v[64:67]
	v_cvt_pk_bf16_f32 v245, v90, v91
	ds_read_b128 v[180:183], v209 offset:28672
	ds_write_b64 v184, v[146:147] offset:49152
	s_waitcnt lgkmcnt(12)
	v_mfma_f32_16x16x32_bf16 v[28:31], v[234:237], v[238:241], v[28:31]
	v_cvt_pk_bf16_f32 v206, v92, v93
	v_mfma_f32_16x16x32_bf16 v[24:27], v[234:237], v[216:219], v[24:27]
	v_cvt_pk_bf16_f32 v207, v94, v95
	ds_read_b128 v[230:233], v246 offset:36864
	global_load_dwordx4 v[148:151], v198, s[8:9]
	s_waitcnt lgkmcnt(12)
	v_mfma_f32_16x16x32_bf16 v[72:75], v[160:163], v[96:99], 0
	v_add_f32_e32 v220, v220, v90
	v_add_f32_e32 v221, v221, v94
	v_mfma_f32_16x16x32_bf16 v[76:79], v[160:163], v[112:115], 0
	v_add_f32_e32 v220, v220, v91
	v_add_f32_e32 v221, v221, v95
	ds_read_b128 v[234:237], v209 offset:30720
	global_load_dwordx4 v[144:147], v199, s[8:9]
	s_waitcnt lgkmcnt(11)
	v_mfma_f32_16x16x32_bf16 v[32:35], v[164:167], v[216:219], v[32:35]
	v_add_f32_e32 v194, v194, v220
	v_add_f32_e32 v195, v195, v221
	v_mfma_f32_16x16x32_bf16 v[36:39], v[164:167], v[238:241], v[36:39]
	v_exp_f32_e32 v64, v64
	v_exp_f32_e32 v68, v68
	ds_read_b128 v[160:163], v201 offset:40960
	global_load_dwordx4 v[136:139], v196, s[6:7]
	s_waitcnt lgkmcnt(10)
	v_mfma_f32_16x16x32_bf16 v[76:79], v[168:171], v[116:119], v[76:79]
	v_exp_f32_e32 v65, v65
	v_mfma_f32_16x16x32_bf16 v[72:75], v[168:171], v[100:103], v[72:75]
	v_exp_f32_e32 v69, v69
	ds_read_b128 v[164:167], v210 offset:16384
	global_load_dwordx4 v[140:143], v197, s[6:7]
	s_waitcnt lgkmcnt(9)
	v_mfma_f32_16x16x32_bf16 v[44:47], v[172:175], v[238:241], v[44:47]
	v_exp_f32_e32 v66, v66
	v_mfma_f32_16x16x32_bf16 v[40:43], v[172:175], v[216:219], v[40:43]
	v_exp_f32_e32 v70, v70
	ds_read_b128 v[168:171], v202 offset:40960
	s_waitcnt lgkmcnt(8)
	v_mfma_f32_16x16x32_bf16 v[72:75], v[176:179], v[104:107], v[72:75]
	v_exp_f32_e32 v67, v67
	v_mfma_f32_16x16x32_bf16 v[76:79], v[176:179], v[120:123], v[76:79]
	v_exp_f32_e32 v71, v71
	ds_read_b128 v[172:175], v210 offset:18432
	s_waitcnt lgkmcnt(7)
	v_mfma_f32_16x16x32_bf16 v[48:51], v[180:183], v[216:219], v[48:51]
	v_add_f32_e32 v220, v64, v65
	v_mfma_f32_16x16x32_bf16 v[52:55], v[180:183], v[238:241], v[52:55]
	v_add_f32_e32 v221, v68, v69
	ds_read_b128 v[176:179], v203 offset:40960
	s_waitcnt lgkmcnt(6)
	v_mfma_f32_16x16x32_bf16 v[76:79], v[230:233], v[124:127], v[76:79]
	v_add_f32_e32 v220, v220, v66
	v_mfma_f32_16x16x32_bf16 v[72:75], v[230:233], v[108:111], v[72:75]
	v_add_f32_e32 v221, v221, v70
	ds_read_b128 v[180:183], v210 offset:20480
	s_waitcnt lgkmcnt(6)
	v_mfma_f32_16x16x32_bf16 v[60:63], v[234:237], v[238:241], v[60:63]
	v_add_f32_e32 v220, v220, v67
	v_mfma_f32_16x16x32_bf16 v[56:59], v[234:237], v[216:219], v[56:59]
	v_add_f32_e32 v221, v221, v71
	ds_read_b128 v[230:233], v246 offset:40960
	s_waitcnt lgkmcnt(6)
	v_mfma_f32_16x16x32_bf16 v[80:83], v[160:163], v[96:99], 0
	v_exp_f32_e32 v72, v72
	v_exp_f32_e32 v76, v76
	v_mfma_f32_16x16x32_bf16 v[84:87], v[160:163], v[112:115], 0
	v_exp_f32_e32 v73, v73
	v_exp_f32_e32 v77, v77
	ds_read_b128 v[234:237], v210 offset:22528
	s_waitcnt lgkmcnt(6)
	v_mfma_f32_16x16x32_bf16 v[0:3], v[164:167], v[242:245], v[0:3]
	v_exp_f32_e32 v74, v74
	v_exp_f32_e32 v78, v78
	v_mfma_f32_16x16x32_bf16 v[4:7], v[164:167], v[204:207], v[4:7]
	v_exp_f32_e32 v75, v75
	v_exp_f32_e32 v79, v79
	ds_read_b128 v[160:163], v201 offset:45056
	s_waitcnt lgkmcnt(6)
	v_mfma_f32_16x16x32_bf16 v[84:87], v[168:171], v[116:119], v[84:87]
	v_add_f32_e32 v220, v220, v72
	v_mfma_f32_16x16x32_bf16 v[80:83], v[168:171], v[100:103], v[80:83]
	v_add_f32_e32 v221, v221, v76
	ds_read_b128 v[164:167], v210 offset:24576
	s_waitcnt lgkmcnt(6)
	v_mfma_f32_16x16x32_bf16 v[12:15], v[172:175], v[204:207], v[12:15]
	v_add_f32_e32 v220, v220, v73
	v_mfma_f32_16x16x32_bf16 v[8:11], v[172:175], v[242:245], v[8:11]
	v_add_f32_e32 v221, v221, v77
	ds_read_b128 v[168:171], v202 offset:45056
	s_waitcnt lgkmcnt(6)
	v_mfma_f32_16x16x32_bf16 v[80:83], v[176:179], v[104:107], v[80:83]
	v_add_f32_e32 v220, v220, v74
	v_mfma_f32_16x16x32_bf16 v[84:87], v[176:179], v[120:123], v[84:87]
	v_add_f32_e32 v221, v221, v78
	ds_read_b128 v[172:175], v210 offset:26624
	s_waitcnt lgkmcnt(6)
	v_mfma_f32_16x16x32_bf16 v[16:19], v[180:183], v[242:245], v[16:19]
	v_add_f32_e32 v220, v220, v75
	v_mfma_f32_16x16x32_bf16 v[20:23], v[180:183], v[204:207], v[20:23]
	v_add_f32_e32 v221, v221, v79
	ds_read_b128 v[176:179], v203 offset:45056
	s_waitcnt lgkmcnt(6)
	v_mfma_f32_16x16x32_bf16 v[84:87], v[230:233], v[124:127], v[84:87]
	v_cvt_pk_bf16_f32 v216, v64, v65
	v_mfma_f32_16x16x32_bf16 v[80:83], v[230:233], v[108:111], v[80:83]
	v_cvt_pk_bf16_f32 v217, v66, v67
	ds_read_b128 v[180:183], v210 offset:28672
	s_waitcnt lgkmcnt(6)
	v_mfma_f32_16x16x32_bf16 v[28:31], v[234:237], v[204:207], v[28:31]
	v_cvt_pk_bf16_f32 v238, v68, v69
	v_mfma_f32_16x16x32_bf16 v[24:27], v[234:237], v[242:245], v[24:27]
	v_cvt_pk_bf16_f32 v239, v70, v71
	ds_read_b128 v[230:233], v246 offset:45056
	s_waitcnt lgkmcnt(6)
	v_mfma_f32_16x16x32_bf16 v[88:91], v[160:163], v[96:99], 0
	v_exp_f32_e32 v80, v80
	v_exp_f32_e32 v84, v84
	v_mfma_f32_16x16x32_bf16 v[92:95], v[160:163], v[112:115], 0
	v_exp_f32_e32 v81, v81
	v_exp_f32_e32 v85, v85
	ds_read_b128 v[234:237], v210 offset:30720
	s_waitcnt lgkmcnt(6)
	v_mfma_f32_16x16x32_bf16 v[32:35], v[164:167], v[242:245], v[32:35]
	v_exp_f32_e32 v82, v82
	v_exp_f32_e32 v86, v86
	v_mfma_f32_16x16x32_bf16 v[36:39], v[164:167], v[204:207], v[36:39]
	v_exp_f32_e32 v83, v83
	v_exp_f32_e32 v87, v87
	s_waitcnt lgkmcnt(5)
	v_mfma_f32_16x16x32_bf16 v[92:95], v[168:171], v[116:119], v[92:95]
	v_add_f32_e32 v220, v220, v80
	v_mfma_f32_16x16x32_bf16 v[88:91], v[168:171], v[100:103], v[88:91]
	v_add_f32_e32 v221, v221, v84
	s_waitcnt lgkmcnt(4)
	v_mfma_f32_16x16x32_bf16 v[44:47], v[172:175], v[204:207], v[44:47]
	v_add_f32_e32 v220, v220, v81
	v_mfma_f32_16x16x32_bf16 v[40:43], v[172:175], v[242:245], v[40:43]
	v_add_f32_e32 v221, v221, v85
	s_waitcnt lgkmcnt(3)
	v_mfma_f32_16x16x32_bf16 v[88:91], v[176:179], v[104:107], v[88:91]
	v_add_f32_e32 v220, v220, v82
	v_mfma_f32_16x16x32_bf16 v[92:95], v[176:179], v[120:123], v[92:95]
	v_add_f32_e32 v221, v221, v86
	s_waitcnt lgkmcnt(2)
	v_mfma_f32_16x16x32_bf16 v[48:51], v[180:183], v[242:245], v[48:51]
	v_add_f32_e32 v220, v220, v83
	v_mfma_f32_16x16x32_bf16 v[52:55], v[180:183], v[204:207], v[52:55]
	v_add_f32_e32 v221, v221, v87
	s_waitcnt lgkmcnt(1)
	v_mfma_f32_16x16x32_bf16 v[92:95], v[230:233], v[124:127], v[92:95]
	v_cvt_pk_bf16_f32 v218, v72, v73
	v_mfma_f32_16x16x32_bf16 v[88:91], v[230:233], v[108:111], v[88:91]
	v_cvt_pk_bf16_f32 v219, v74, v75
	s_waitcnt lgkmcnt(0)
	v_mfma_f32_16x16x32_bf16 v[60:63], v[234:237], v[204:207], v[60:63]
	v_cvt_pk_bf16_f32 v240, v76, v77
	v_mfma_f32_16x16x32_bf16 v[56:59], v[234:237], v[242:245], v[56:59]
	v_cvt_pk_bf16_f32 v241, v78, v79
	s_waitcnt lgkmcnt(0)
	s_barrier
	ds_read_b128 v[160:163], v201 offset:49152
	ds_read_b128 v[164:167], v209 offset:32768
	ds_read_b128 v[168:171], v202 offset:49152
	ds_read_b128 v[172:175], v209 offset:34816
	ds_read_b128 v[176:179], v203 offset:49152
	ds_read_b128 v[180:183], v209 offset:36864
	ds_read_b128 v[230:233], v246 offset:49152
	s_waitcnt lgkmcnt(6)
	v_mfma_f32_16x16x32_bf16 v[64:67], v[160:163], v[96:99], 0
	v_mfma_f32_16x16x32_bf16 v[68:71], v[160:163], v[112:115], 0
	ds_read_b128 v[234:237], v209 offset:38912
	s_add_u32 s8, s16, 0x3bc00300
	s_addc_u32 s9, s17, 0
	s_add_u32 s6, s15, 0x23a70000
	s_addc_u32 s7, s14, 0
	s_waitcnt lgkmcnt(6)
	v_mfma_f32_16x16x32_bf16 v[0:3], v[164:167], v[216:219], v[0:3]
	v_mfma_f32_16x16x32_bf16 v[4:7], v[164:167], v[238:241], v[4:7]
	ds_read_b128 v[160:163], v201 offset:53248
	s_waitcnt vmcnt(4)
	ds_write_b128 v225, v[152:155] offset:16384
	s_waitcnt lgkmcnt(7)
	v_mfma_f32_16x16x32_bf16 v[68:71], v[168:171], v[116:119], v[68:71]
	v_mfma_f32_16x16x32_bf16 v[64:67], v[168:171], v[100:103], v[64:67]
	ds_read_b128 v[164:167], v209 offset:40960
	ds_write_b128 v226, v[156:159] offset:16384
	s_waitcnt lgkmcnt(8)
	v_mfma_f32_16x16x32_bf16 v[12:15], v[172:175], v[238:241], v[12:15]
	v_mfma_f32_16x16x32_bf16 v[8:11], v[172:175], v[216:219], v[8:11]
	ds_read_b128 v[168:171], v202 offset:53248
	ds_write_b64 v227, v[132:133] offset:0
	s_waitcnt lgkmcnt(9)
	v_mfma_f32_16x16x32_bf16 v[64:67], v[176:179], v[104:107], v[64:67]
	v_exp_f32_e32 v88, v88
	v_exp_f32_e32 v92, v92
	v_mfma_f32_16x16x32_bf16 v[68:71], v[176:179], v[120:123], v[68:71]
	v_cvt_pk_bf16_f32 v242, v80, v81
	v_exp_f32_e32 v89, v89
	ds_read_b128 v[172:175], v209 offset:43008
	ds_write_b64 v228, v[134:135] offset:0
	s_waitcnt lgkmcnt(10)
	v_mfma_f32_16x16x32_bf16 v[16:19], v[180:183], v[216:219], v[16:19]
	v_exp_f32_e32 v93, v93
	v_cvt_pk_bf16_f32 v243, v82, v83
	v_mfma_f32_16x16x32_bf16 v[20:23], v[180:183], v[238:241], v[20:23]
	v_exp_f32_e32 v90, v90
	v_exp_f32_e32 v94, v94
	ds_read_b128 v[176:179], v203 offset:53248
	ds_write_b64 v229, v[128:129] offset:0
	s_waitcnt lgkmcnt(11)
	v_mfma_f32_16x16x32_bf16 v[68:71], v[230:233], v[124:127], v[68:71]
	v_cvt_pk_bf16_f32 v204, v84, v85
	v_exp_f32_e32 v91, v91
	v_mfma_f32_16x16x32_bf16 v[64:67], v[230:233], v[108:111], v[64:67]
	v_exp_f32_e32 v95, v95
	v_cvt_pk_bf16_f32 v205, v86, v87
	ds_read_b128 v[180:183], v209 offset:45056
	ds_write_b64 v184, v[130:131] offset:0
	s_waitcnt lgkmcnt(12)
	v_mfma_f32_16x16x32_bf16 v[28:31], v[234:237], v[238:241], v[28:31]
	v_add_f32_e32 v220, v220, v88
	v_add_f32_e32 v221, v221, v92
	v_mfma_f32_16x16x32_bf16 v[24:27], v[234:237], v[216:219], v[24:27]
	v_add_f32_e32 v220, v220, v89
	v_add_f32_e32 v221, v221, v93
	ds_read_b128 v[230:233], v246 offset:53248
	global_load_dwordx4 v[132:135], v198, s[8:9]
	s_waitcnt lgkmcnt(12)
	v_mfma_f32_16x16x32_bf16 v[72:75], v[160:163], v[96:99], 0
	v_cvt_pk_bf16_f32 v244, v88, v89
	v_cvt_pk_bf16_f32 v245, v90, v91
	v_mfma_f32_16x16x32_bf16 v[76:79], v[160:163], v[112:115], 0
	v_cvt_pk_bf16_f32 v206, v92, v93
	v_cvt_pk_bf16_f32 v207, v94, v95
	ds_read_b128 v[234:237], v209 offset:47104
	global_load_dwordx4 v[128:131], v199, s[8:9]
	s_waitcnt lgkmcnt(11)
	v_mfma_f32_16x16x32_bf16 v[32:35], v[164:167], v[216:219], v[32:35]
	v_add_f32_e32 v220, v220, v90
	v_add_f32_e32 v221, v221, v94
	v_mfma_f32_16x16x32_bf16 v[36:39], v[164:167], v[238:241], v[36:39]
	v_add_f32_e32 v220, v220, v91
	v_add_f32_e32 v221, v221, v95
	ds_read_b128 v[160:163], v201 offset:57344
	global_load_dwordx4 v[152:155], v196, s[6:7]
	s_waitcnt lgkmcnt(10)
	v_mfma_f32_16x16x32_bf16 v[76:79], v[168:171], v[116:119], v[76:79]
	v_add_f32_e32 v194, v194, v220
	v_add_f32_e32 v195, v195, v221
	v_mfma_f32_16x16x32_bf16 v[72:75], v[168:171], v[100:103], v[72:75]
	v_exp_f32_e32 v64, v64
	v_exp_f32_e32 v68, v68
	ds_read_b128 v[164:167], v210 offset:32768
	global_load_dwordx4 v[156:159], v197, s[6:7]
	s_waitcnt lgkmcnt(9)
	v_mfma_f32_16x16x32_bf16 v[44:47], v[172:175], v[238:241], v[44:47]
	v_exp_f32_e32 v65, v65
	v_exp_f32_e32 v69, v69
	v_mfma_f32_16x16x32_bf16 v[40:43], v[172:175], v[216:219], v[40:43]
	v_exp_f32_e32 v66, v66
	v_exp_f32_e32 v70, v70
	ds_read_b128 v[168:171], v202 offset:57344
	s_waitcnt lgkmcnt(8)
	v_mfma_f32_16x16x32_bf16 v[72:75], v[176:179], v[104:107], v[72:75]
	v_exp_f32_e32 v67, v67
	v_mfma_f32_16x16x32_bf16 v[76:79], v[176:179], v[120:123], v[76:79]
	v_exp_f32_e32 v71, v71
	ds_read_b128 v[172:175], v210 offset:34816
	s_waitcnt lgkmcnt(7)
	v_mfma_f32_16x16x32_bf16 v[48:51], v[180:183], v[216:219], v[48:51]
	v_add_f32_e32 v220, v64, v65
	v_mfma_f32_16x16x32_bf16 v[52:55], v[180:183], v[238:241], v[52:55]
	v_add_f32_e32 v221, v68, v69
	ds_read_b128 v[176:179], v203 offset:57344
	s_waitcnt lgkmcnt(6)
	v_mfma_f32_16x16x32_bf16 v[76:79], v[230:233], v[124:127], v[76:79]
	v_add_f32_e32 v220, v220, v66
	v_mfma_f32_16x16x32_bf16 v[72:75], v[230:233], v[108:111], v[72:75]
	v_add_f32_e32 v221, v221, v70
	ds_read_b128 v[180:183], v210 offset:36864
	s_waitcnt lgkmcnt(6)
	v_mfma_f32_16x16x32_bf16 v[60:63], v[234:237], v[238:241], v[60:63]
	v_add_f32_e32 v220, v220, v67
	v_mfma_f32_16x16x32_bf16 v[56:59], v[234:237], v[216:219], v[56:59]
	v_add_f32_e32 v221, v221, v71
	ds_read_b128 v[230:233], v246 offset:57344
	s_waitcnt lgkmcnt(6)
	v_mfma_f32_16x16x32_bf16 v[80:83], v[160:163], v[96:99], 0
	v_exp_f32_e32 v72, v72
	v_exp_f32_e32 v76, v76
	v_mfma_f32_16x16x32_bf16 v[84:87], v[160:163], v[112:115], 0
	v_exp_f32_e32 v73, v73
	v_exp_f32_e32 v77, v77
	ds_read_b128 v[234:237], v210 offset:38912
	s_waitcnt lgkmcnt(6)
	v_mfma_f32_16x16x32_bf16 v[0:3], v[164:167], v[242:245], v[0:3]
	v_exp_f32_e32 v74, v74
	v_exp_f32_e32 v78, v78
	v_mfma_f32_16x16x32_bf16 v[4:7], v[164:167], v[204:207], v[4:7]
	v_exp_f32_e32 v75, v75
	v_exp_f32_e32 v79, v79
	ds_read_b128 v[160:163], v201 offset:61440
	s_waitcnt lgkmcnt(6)
	v_mfma_f32_16x16x32_bf16 v[84:87], v[168:171], v[116:119], v[84:87]
	v_add_f32_e32 v220, v220, v72
	v_mfma_f32_16x16x32_bf16 v[80:83], v[168:171], v[100:103], v[80:83]
	v_add_f32_e32 v221, v221, v76
	ds_read_b128 v[164:167], v210 offset:40960
	s_waitcnt lgkmcnt(6)
	v_mfma_f32_16x16x32_bf16 v[12:15], v[172:175], v[204:207], v[12:15]
	v_add_f32_e32 v220, v220, v73
	v_mfma_f32_16x16x32_bf16 v[8:11], v[172:175], v[242:245], v[8:11]
	v_add_f32_e32 v221, v221, v77
	ds_read_b128 v[168:171], v202 offset:61440
	s_waitcnt lgkmcnt(6)
	v_mfma_f32_16x16x32_bf16 v[80:83], v[176:179], v[104:107], v[80:83]
	v_add_f32_e32 v220, v220, v74
	v_mfma_f32_16x16x32_bf16 v[84:87], v[176:179], v[120:123], v[84:87]
	v_add_f32_e32 v221, v221, v78
	ds_read_b128 v[172:175], v210 offset:43008
	s_waitcnt lgkmcnt(6)
	v_mfma_f32_16x16x32_bf16 v[16:19], v[180:183], v[242:245], v[16:19]
	v_add_f32_e32 v220, v220, v75
	v_mfma_f32_16x16x32_bf16 v[20:23], v[180:183], v[204:207], v[20:23]
	v_add_f32_e32 v221, v221, v79
	ds_read_b128 v[176:179], v203 offset:61440
	s_waitcnt lgkmcnt(6)
	v_mfma_f32_16x16x32_bf16 v[84:87], v[230:233], v[124:127], v[84:87]
	v_cvt_pk_bf16_f32 v216, v64, v65
	v_mfma_f32_16x16x32_bf16 v[80:83], v[230:233], v[108:111], v[80:83]
	v_cvt_pk_bf16_f32 v217, v66, v67
	ds_read_b128 v[180:183], v210 offset:45056
	s_waitcnt lgkmcnt(6)
	v_mfma_f32_16x16x32_bf16 v[28:31], v[234:237], v[204:207], v[28:31]
	v_cvt_pk_bf16_f32 v238, v68, v69
	v_mfma_f32_16x16x32_bf16 v[24:27], v[234:237], v[242:245], v[24:27]
	v_cvt_pk_bf16_f32 v239, v70, v71
	ds_read_b128 v[230:233], v246 offset:61440
	s_waitcnt lgkmcnt(6)
	v_mfma_f32_16x16x32_bf16 v[88:91], v[160:163], v[96:99], 0
	v_exp_f32_e32 v80, v80
	v_exp_f32_e32 v84, v84
	v_mfma_f32_16x16x32_bf16 v[92:95], v[160:163], v[112:115], 0
	v_exp_f32_e32 v81, v81
	v_exp_f32_e32 v85, v85
	ds_read_b128 v[234:237], v210 offset:47104
	s_waitcnt lgkmcnt(6)
	v_mfma_f32_16x16x32_bf16 v[32:35], v[164:167], v[242:245], v[32:35]
	v_exp_f32_e32 v82, v82
	v_exp_f32_e32 v86, v86
	v_mfma_f32_16x16x32_bf16 v[36:39], v[164:167], v[204:207], v[36:39]
	v_exp_f32_e32 v83, v83
	v_exp_f32_e32 v87, v87
	ds_read_b128 v[160:163], v201 offset:0
	s_waitcnt lgkmcnt(6)
	v_mfma_f32_16x16x32_bf16 v[92:95], v[168:171], v[116:119], v[92:95]
	v_add_f32_e32 v220, v220, v80
	v_mfma_f32_16x16x32_bf16 v[88:91], v[168:171], v[100:103], v[88:91]
	v_add_f32_e32 v221, v221, v84
	ds_read_b128 v[164:167], v209 offset:49152
	s_waitcnt lgkmcnt(6)
	v_mfma_f32_16x16x32_bf16 v[44:47], v[172:175], v[204:207], v[44:47]
	v_add_f32_e32 v220, v220, v81
	v_mfma_f32_16x16x32_bf16 v[40:43], v[172:175], v[242:245], v[40:43]
	v_add_f32_e32 v221, v221, v85
	ds_read_b128 v[168:171], v202 offset:0
	s_waitcnt lgkmcnt(6)
	v_mfma_f32_16x16x32_bf16 v[88:91], v[176:179], v[104:107], v[88:91]
	v_add_f32_e32 v220, v220, v82
	v_mfma_f32_16x16x32_bf16 v[92:95], v[176:179], v[120:123], v[92:95]
	v_add_f32_e32 v221, v221, v86
	ds_read_b128 v[172:175], v209 offset:51200
	s_waitcnt lgkmcnt(6)
	v_mfma_f32_16x16x32_bf16 v[48:51], v[180:183], v[242:245], v[48:51]
	v_add_f32_e32 v220, v220, v83
	v_mfma_f32_16x16x32_bf16 v[52:55], v[180:183], v[204:207], v[52:55]
	v_add_f32_e32 v221, v221, v87
	ds_read_b128 v[176:179], v203 offset:0
	s_waitcnt lgkmcnt(6)
	v_mfma_f32_16x16x32_bf16 v[92:95], v[230:233], v[124:127], v[92:95]
	v_cvt_pk_bf16_f32 v218, v72, v73
	v_mfma_f32_16x16x32_bf16 v[88:91], v[230:233], v[108:111], v[88:91]
	v_cvt_pk_bf16_f32 v219, v74, v75
	ds_read_b128 v[180:183], v209 offset:53248
	s_waitcnt lgkmcnt(6)
	v_mfma_f32_16x16x32_bf16 v[60:63], v[234:237], v[204:207], v[60:63]
	v_cvt_pk_bf16_f32 v240, v76, v77
	v_mfma_f32_16x16x32_bf16 v[56:59], v[234:237], v[242:245], v[56:59]
	v_cvt_pk_bf16_f32 v241, v78, v79
	ds_read_b128 v[230:233], v246 offset:0
	s_waitcnt lgkmcnt(6)
	v_mfma_f32_16x16x32_bf16 v[64:67], v[160:163], v[96:99], 0
	v_exp_f32_e32 v88, v88
	v_exp_f32_e32 v92, v92
	v_mfma_f32_16x16x32_bf16 v[68:71], v[160:163], v[112:115], 0
	v_cvt_pk_bf16_f32 v242, v80, v81
	v_exp_f32_e32 v89, v89
	ds_read_b128 v[234:237], v209 offset:55296
	s_add_u32 s8, s16, 0x3bc00380
	s_addc_u32 s9, s17, 0
	s_add_u32 s6, s15, 0x23a80000
	s_addc_u32 s7, s14, 0
	s_waitcnt lgkmcnt(6)
	v_mfma_f32_16x16x32_bf16 v[0:3], v[164:167], v[216:219], v[0:3]
	v_exp_f32_e32 v93, v93
	v_cvt_pk_bf16_f32 v243, v82, v83
	v_mfma_f32_16x16x32_bf16 v[4:7], v[164:167], v[238:241], v[4:7]
	v_exp_f32_e32 v90, v90
	v_exp_f32_e32 v94, v94
	ds_read_b128 v[160:163], v201 offset:4096
	s_waitcnt vmcnt(4)
	ds_write_b128 v225, v[136:139] offset:32768
	s_waitcnt lgkmcnt(7)
	v_mfma_f32_16x16x32_bf16 v[68:71], v[168:171], v[116:119], v[68:71]
	v_cvt_pk_bf16_f32 v204, v84, v85
	v_mfma_f32_16x16x32_bf16 v[64:67], v[168:171], v[100:103], v[64:67]
	v_exp_f32_e32 v91, v91
	ds_read_b128 v[164:167], v209 offset:57344
	ds_write_b128 v226, v[140:143] offset:32768
	s_waitcnt lgkmcnt(8)
	v_mfma_f32_16x16x32_bf16 v[12:15], v[172:175], v[238:241], v[12:15]
	v_exp_f32_e32 v95, v95
	v_mfma_f32_16x16x32_bf16 v[8:11], v[172:175], v[216:219], v[8:11]
	v_cvt_pk_bf16_f32 v205, v86, v87
	ds_read_b128 v[168:171], v202 offset:4096
	ds_write_b64 v227, v[148:149] offset:16384
	s_waitcnt lgkmcnt(9)
	v_mfma_f32_16x16x32_bf16 v[64:67], v[176:179], v[104:107], v[64:67]
	v_add_f32_e32 v220, v220, v88
	v_mfma_f32_16x16x32_bf16 v[68:71], v[176:179], v[120:123], v[68:71]
	v_add_f32_e32 v221, v221, v92
	ds_read_b128 v[172:175], v209 offset:59392
	ds_write_b64 v228, v[150:151] offset:16384
	s_waitcnt lgkmcnt(10)
	v_mfma_f32_16x16x32_bf16 v[16:19], v[180:183], v[216:219], v[16:19]
	v_add_f32_e32 v220, v220, v89
	v_mfma_f32_16x16x32_bf16 v[20:23], v[180:183], v[238:241], v[20:23]
	v_add_f32_e32 v221, v221, v93
	ds_read_b128 v[176:179], v203 offset:4096
	ds_write_b64 v229, v[144:145] offset:16384
	s_waitcnt lgkmcnt(11)
	v_mfma_f32_16x16x32_bf16 v[68:71], v[230:233], v[124:127], v[68:71]
	v_cvt_pk_bf16_f32 v244, v88, v89
	v_mfma_f32_16x16x32_bf16 v[64:67], v[230:233], v[108:111], v[64:67]
	v_cvt_pk_bf16_f32 v245, v90, v91
	ds_read_b128 v[180:183], v209 offset:61440
	ds_write_b64 v184, v[146:147] offset:16384
	s_waitcnt lgkmcnt(12)
	v_mfma_f32_16x16x32_bf16 v[28:31], v[234:237], v[238:241], v[28:31]
	v_cvt_pk_bf16_f32 v206, v92, v93
	v_mfma_f32_16x16x32_bf16 v[24:27], v[234:237], v[216:219], v[24:27]
	v_cvt_pk_bf16_f32 v207, v94, v95
	ds_read_b128 v[230:233], v246 offset:4096
	global_load_dwordx4 v[148:151], v198, s[8:9]
	s_waitcnt lgkmcnt(12)
	v_mfma_f32_16x16x32_bf16 v[72:75], v[160:163], v[96:99], 0
	v_add_f32_e32 v220, v220, v90
	v_add_f32_e32 v221, v221, v94
	v_mfma_f32_16x16x32_bf16 v[76:79], v[160:163], v[112:115], 0
	v_add_f32_e32 v220, v220, v91
	v_add_f32_e32 v221, v221, v95
	ds_read_b128 v[234:237], v209 offset:63488
	global_load_dwordx4 v[144:147], v199, s[8:9]
	s_waitcnt lgkmcnt(11)
	v_mfma_f32_16x16x32_bf16 v[32:35], v[164:167], v[216:219], v[32:35]
	v_add_f32_e32 v194, v194, v220
	v_add_f32_e32 v195, v195, v221
	v_mfma_f32_16x16x32_bf16 v[36:39], v[164:167], v[238:241], v[36:39]
	v_exp_f32_e32 v64, v64
	v_exp_f32_e32 v68, v68
	ds_read_b128 v[160:163], v201 offset:8192
	global_load_dwordx4 v[136:139], v196, s[6:7]
	s_waitcnt lgkmcnt(10)
	v_mfma_f32_16x16x32_bf16 v[76:79], v[168:171], v[116:119], v[76:79]
	v_exp_f32_e32 v65, v65
	v_mfma_f32_16x16x32_bf16 v[72:75], v[168:171], v[100:103], v[72:75]
	v_exp_f32_e32 v69, v69
	ds_read_b128 v[164:167], v210 offset:49152
	global_load_dwordx4 v[140:143], v197, s[6:7]
	s_waitcnt lgkmcnt(9)
	v_mfma_f32_16x16x32_bf16 v[44:47], v[172:175], v[238:241], v[44:47]
	v_exp_f32_e32 v66, v66
	v_mfma_f32_16x16x32_bf16 v[40:43], v[172:175], v[216:219], v[40:43]
	v_exp_f32_e32 v70, v70
	ds_read_b128 v[168:171], v202 offset:8192
	s_waitcnt lgkmcnt(8)
	v_mfma_f32_16x16x32_bf16 v[72:75], v[176:179], v[104:107], v[72:75]
	v_exp_f32_e32 v67, v67
	v_mfma_f32_16x16x32_bf16 v[76:79], v[176:179], v[120:123], v[76:79]
	v_exp_f32_e32 v71, v71
	ds_read_b128 v[172:175], v210 offset:51200
	s_waitcnt lgkmcnt(7)
	v_mfma_f32_16x16x32_bf16 v[48:51], v[180:183], v[216:219], v[48:51]
	v_add_f32_e32 v220, v64, v65
	v_mfma_f32_16x16x32_bf16 v[52:55], v[180:183], v[238:241], v[52:55]
	v_add_f32_e32 v221, v68, v69
	ds_read_b128 v[176:179], v203 offset:8192
	s_waitcnt lgkmcnt(6)
	v_mfma_f32_16x16x32_bf16 v[76:79], v[230:233], v[124:127], v[76:79]
	v_add_f32_e32 v220, v220, v66
	v_mfma_f32_16x16x32_bf16 v[72:75], v[230:233], v[108:111], v[72:75]
	v_add_f32_e32 v221, v221, v70
	ds_read_b128 v[180:183], v210 offset:53248
	s_waitcnt lgkmcnt(6)
	v_mfma_f32_16x16x32_bf16 v[60:63], v[234:237], v[238:241], v[60:63]
	v_add_f32_e32 v220, v220, v67
	v_mfma_f32_16x16x32_bf16 v[56:59], v[234:237], v[216:219], v[56:59]
	v_add_f32_e32 v221, v221, v71
	ds_read_b128 v[230:233], v246 offset:8192
	s_waitcnt lgkmcnt(6)
	v_mfma_f32_16x16x32_bf16 v[80:83], v[160:163], v[96:99], 0
	v_exp_f32_e32 v72, v72
	v_exp_f32_e32 v76, v76
	v_mfma_f32_16x16x32_bf16 v[84:87], v[160:163], v[112:115], 0
	v_exp_f32_e32 v73, v73
	v_exp_f32_e32 v77, v77
	ds_read_b128 v[234:237], v210 offset:55296
	s_waitcnt lgkmcnt(6)
	v_mfma_f32_16x16x32_bf16 v[0:3], v[164:167], v[242:245], v[0:3]
	v_exp_f32_e32 v74, v74
	v_exp_f32_e32 v78, v78
	v_mfma_f32_16x16x32_bf16 v[4:7], v[164:167], v[204:207], v[4:7]
	v_exp_f32_e32 v75, v75
	v_exp_f32_e32 v79, v79
	ds_read_b128 v[160:163], v201 offset:12288
	s_waitcnt lgkmcnt(6)
	v_mfma_f32_16x16x32_bf16 v[84:87], v[168:171], v[116:119], v[84:87]
	v_add_f32_e32 v220, v220, v72
	v_mfma_f32_16x16x32_bf16 v[80:83], v[168:171], v[100:103], v[80:83]
	v_add_f32_e32 v221, v221, v76
	ds_read_b128 v[164:167], v210 offset:57344
	s_waitcnt lgkmcnt(6)
	v_mfma_f32_16x16x32_bf16 v[12:15], v[172:175], v[204:207], v[12:15]
	v_add_f32_e32 v220, v220, v73
	v_mfma_f32_16x16x32_bf16 v[8:11], v[172:175], v[242:245], v[8:11]
	v_add_f32_e32 v221, v221, v77
	ds_read_b128 v[168:171], v202 offset:12288
	s_waitcnt lgkmcnt(6)
	v_mfma_f32_16x16x32_bf16 v[80:83], v[176:179], v[104:107], v[80:83]
	v_add_f32_e32 v220, v220, v74
	v_mfma_f32_16x16x32_bf16 v[84:87], v[176:179], v[120:123], v[84:87]
	v_add_f32_e32 v221, v221, v78
	ds_read_b128 v[172:175], v210 offset:59392
	s_add_u32 s10, s10, 0x200
	s_addc_u32 s11, s11, 0
	s_add_u32 s12, s12, 0x40000
	s_addc_u32 s13, s13, 0
	s_add_i32 s4, s4, 4
	s_cmpk_lt_u32 s4, 0x104
	s_cselect_b64 s[6:7], -1, 0
	s_and_b64 s[6:7], s[0:1], s[6:7]
	s_and_b64 vcc, exec, s[6:7]
	s_waitcnt lgkmcnt(6)
	v_mfma_f32_16x16x32_bf16 v[16:19], v[180:183], v[242:245], v[16:19]
	v_add_f32_e32 v220, v220, v75
	v_mfma_f32_16x16x32_bf16 v[20:23], v[180:183], v[204:207], v[20:23]
	v_add_f32_e32 v221, v221, v79
	ds_read_b128 v[176:179], v203 offset:12288
	s_waitcnt lgkmcnt(6)
	v_mfma_f32_16x16x32_bf16 v[84:87], v[230:233], v[124:127], v[84:87]
	v_cvt_pk_bf16_f32 v216, v64, v65
	v_mfma_f32_16x16x32_bf16 v[80:83], v[230:233], v[108:111], v[80:83]
	v_cvt_pk_bf16_f32 v217, v66, v67
	ds_read_b128 v[180:183], v210 offset:61440
	s_waitcnt lgkmcnt(6)
	v_mfma_f32_16x16x32_bf16 v[28:31], v[234:237], v[204:207], v[28:31]
	v_cvt_pk_bf16_f32 v238, v68, v69
	v_mfma_f32_16x16x32_bf16 v[24:27], v[234:237], v[242:245], v[24:27]
	v_cvt_pk_bf16_f32 v239, v70, v71
	ds_read_b128 v[230:233], v246 offset:12288
	s_waitcnt lgkmcnt(6)
	v_mfma_f32_16x16x32_bf16 v[88:91], v[160:163], v[96:99], 0
	v_exp_f32_e32 v80, v80
	v_exp_f32_e32 v84, v84
	v_mfma_f32_16x16x32_bf16 v[92:95], v[160:163], v[112:115], 0
	v_exp_f32_e32 v81, v81
	v_exp_f32_e32 v85, v85
	ds_read_b128 v[234:237], v210 offset:63488
	s_waitcnt lgkmcnt(6)
	v_mfma_f32_16x16x32_bf16 v[32:35], v[164:167], v[242:245], v[32:35]
	v_exp_f32_e32 v82, v82
	v_exp_f32_e32 v86, v86
	v_mfma_f32_16x16x32_bf16 v[36:39], v[164:167], v[204:207], v[36:39]
	v_exp_f32_e32 v83, v83
	v_exp_f32_e32 v87, v87
	s_waitcnt lgkmcnt(5)
	v_mfma_f32_16x16x32_bf16 v[92:95], v[168:171], v[116:119], v[92:95]
	v_add_f32_e32 v220, v220, v80
	v_mfma_f32_16x16x32_bf16 v[88:91], v[168:171], v[100:103], v[88:91]
	v_add_f32_e32 v221, v221, v84
	s_waitcnt lgkmcnt(4)
	v_mfma_f32_16x16x32_bf16 v[44:47], v[172:175], v[204:207], v[44:47]
	v_add_f32_e32 v220, v220, v81
	v_mfma_f32_16x16x32_bf16 v[40:43], v[172:175], v[242:245], v[40:43]
	v_add_f32_e32 v221, v221, v85
	s_waitcnt lgkmcnt(3)
	v_mfma_f32_16x16x32_bf16 v[88:91], v[176:179], v[104:107], v[88:91]
	v_add_f32_e32 v220, v220, v82
	v_mfma_f32_16x16x32_bf16 v[92:95], v[176:179], v[120:123], v[92:95]
	v_add_f32_e32 v221, v221, v86
	s_waitcnt lgkmcnt(2)
	v_mfma_f32_16x16x32_bf16 v[48:51], v[180:183], v[242:245], v[48:51]
	v_add_f32_e32 v220, v220, v83
	v_mfma_f32_16x16x32_bf16 v[52:55], v[180:183], v[204:207], v[52:55]
	v_add_f32_e32 v221, v221, v87
	s_waitcnt lgkmcnt(1)
	v_mfma_f32_16x16x32_bf16 v[92:95], v[230:233], v[124:127], v[92:95]
	v_cvt_pk_bf16_f32 v218, v72, v73
	v_mfma_f32_16x16x32_bf16 v[88:91], v[230:233], v[108:111], v[88:91]
	v_cvt_pk_bf16_f32 v219, v74, v75
	s_waitcnt lgkmcnt(0)
	v_mfma_f32_16x16x32_bf16 v[60:63], v[234:237], v[204:207], v[60:63]
	v_cvt_pk_bf16_f32 v240, v76, v77
	v_mfma_f32_16x16x32_bf16 v[56:59], v[234:237], v[242:245], v[56:59]
	v_cvt_pk_bf16_f32 v241, v78, v79
	s_cbranch_vccnz .LBB0_734
	s_waitcnt vmcnt(0)
	s_nop 7
	s_nop 7
	ds_swizzle_b32 v64, v194 offset:swizzle(SWAP,16)
	s_waitcnt lgkmcnt(0)
	v_add_f32_e32 v194, v194, v64
	v_mov_b32_e32 v65, v194
	s_nop 1
	v_permlane32_swap_b32_e32 v194, v65
	v_add_f32_e32 v194, v194, v65
	s_nop 0
	v_rcp_f32_e32 v66, v194
	ds_swizzle_b32 v64, v195 offset:swizzle(SWAP,16)
	s_waitcnt lgkmcnt(0)
	v_add_f32_e32 v195, v195, v64
	v_mov_b32_e32 v65, v195
	s_nop 1
	v_permlane32_swap_b32_e32 v195, v65
	v_add_f32_e32 v195, v195, v65
	s_nop 0
	v_rcp_f32_e32 v67, v195
	v_readlane_b32 s100, v250, 8
	v_mbcnt_lo_u32_b32 v68, -1, 0
	v_mbcnt_hi_u32_b32 v68, -1, v68
	v_and_b32_e32 v69, 15, v68
	v_lshrrev_b32_e32 v70, 4, v68
	s_lshr_b32 s101, s100, 1
	v_add_u32_e32 v69, s101, v69
	v_lshlrev_b32_e32 v69, 12, v69
	v_and_b32_e32 v71, 1, v70
	v_lshlrev_b32_e32 v71, 5, v71
	v_and_b32_e32 v70, 2, v70
	v_lshl_add_u32 v71, v70, 3, v71
	v_add_u32_e32 v70, v69, v71
	v_add_u32_e32 v71, 0x10000, v70
	v_mul_f32_e32 v0, v0, v66
	v_mul_f32_e32 v1, v1, v66
	v_mul_f32_e32 v2, v2, v66
	v_mul_f32_e32 v3, v3, v66
	v_mul_f32_e32 v8, v8, v66
	v_mul_f32_e32 v9, v9, v66
	v_mul_f32_e32 v10, v10, v66
	v_mul_f32_e32 v11, v11, v66
	v_cvt_pk_bf16_f32 v72, v0, v1
	v_cvt_pk_bf16_f32 v73, v2, v3
	v_cvt_pk_bf16_f32 v74, v8, v9
	v_cvt_pk_bf16_f32 v75, v10, v11
	s_nop 1
	v_permlane16_swap_b32_e32 v72, v74
	v_permlane16_swap_b32_e32 v73, v75
	s_nop 1
	global_store_dwordx4 v70, v[72:75], s[58:59] offset:0
	v_mul_f32_e32 v16, v16, v66
	v_mul_f32_e32 v17, v17, v66
	v_mul_f32_e32 v18, v18, v66
	v_mul_f32_e32 v19, v19, v66
	v_mul_f32_e32 v24, v24, v66
	v_mul_f32_e32 v25, v25, v66
	v_mul_f32_e32 v26, v26, v66
	v_mul_f32_e32 v27, v27, v66
	v_cvt_pk_bf16_f32 v76, v16, v17
	v_cvt_pk_bf16_f32 v77, v18, v19
	v_cvt_pk_bf16_f32 v78, v24, v25
	v_cvt_pk_bf16_f32 v79, v26, v27
	s_nop 1
	v_permlane16_swap_b32_e32 v76, v78
	v_permlane16_swap_b32_e32 v77, v79
	s_nop 1
	global_store_dwordx4 v70, v[76:79], s[58:59] offset:64
	v_mul_f32_e32 v32, v32, v66
	v_mul_f32_e32 v33, v33, v66
	v_mul_f32_e32 v34, v34, v66
	v_mul_f32_e32 v35, v35, v66
	v_mul_f32_e32 v40, v40, v66
	v_mul_f32_e32 v41, v41, v66
	v_mul_f32_e32 v42, v42, v66
	v_mul_f32_e32 v43, v43, v66
	v_cvt_pk_bf16_f32 v80, v32, v33
	v_cvt_pk_bf16_f32 v81, v34, v35
	v_cvt_pk_bf16_f32 v82, v40, v41
	v_cvt_pk_bf16_f32 v83, v42, v43
	s_nop 1
	v_permlane16_swap_b32_e32 v80, v82
	v_permlane16_swap_b32_e32 v81, v83
	s_nop 1
	global_store_dwordx4 v70, v[80:83], s[58:59] offset:128
	v_mul_f32_e32 v48, v48, v66
	v_mul_f32_e32 v49, v49, v66
	v_mul_f32_e32 v50, v50, v66
	v_mul_f32_e32 v51, v51, v66
	v_mul_f32_e32 v56, v56, v66
	v_mul_f32_e32 v57, v57, v66
	v_mul_f32_e32 v58, v58, v66
	v_mul_f32_e32 v59, v59, v66
	v_cvt_pk_bf16_f32 v84, v48, v49
	v_cvt_pk_bf16_f32 v85, v50, v51
	v_cvt_pk_bf16_f32 v86, v56, v57
	v_cvt_pk_bf16_f32 v87, v58, v59
	s_nop 1
	v_permlane16_swap_b32_e32 v84, v86
	v_permlane16_swap_b32_e32 v85, v87
	s_nop 1
	global_store_dwordx4 v70, v[84:87], s[58:59] offset:192
	v_mul_f32_e32 v4, v4, v67
	v_mul_f32_e32 v5, v5, v67
	v_mul_f32_e32 v6, v6, v67
	v_mul_f32_e32 v7, v7, v67
	v_mul_f32_e32 v12, v12, v67
	v_mul_f32_e32 v13, v13, v67
	v_mul_f32_e32 v14, v14, v67
	v_mul_f32_e32 v15, v15, v67
	v_cvt_pk_bf16_f32 v88, v4, v5
	v_cvt_pk_bf16_f32 v89, v6, v7
	v_cvt_pk_bf16_f32 v90, v12, v13
	v_cvt_pk_bf16_f32 v91, v14, v15
	s_nop 1
	v_permlane16_swap_b32_e32 v88, v90
	v_permlane16_swap_b32_e32 v89, v91
	s_nop 1
	global_store_dwordx4 v71, v[88:91], s[58:59] offset:0
	v_mul_f32_e32 v20, v20, v67
	v_mul_f32_e32 v21, v21, v67
	v_mul_f32_e32 v22, v22, v67
	v_mul_f32_e32 v23, v23, v67
	v_mul_f32_e32 v28, v28, v67
	v_mul_f32_e32 v29, v29, v67
	v_mul_f32_e32 v30, v30, v67
	v_mul_f32_e32 v31, v31, v67
	v_cvt_pk_bf16_f32 v92, v20, v21
	v_cvt_pk_bf16_f32 v93, v22, v23
	v_cvt_pk_bf16_f32 v94, v28, v29
	v_cvt_pk_bf16_f32 v95, v30, v31
	s_nop 1
	v_permlane16_swap_b32_e32 v92, v94
	v_permlane16_swap_b32_e32 v93, v95
	s_nop 1
	global_store_dwordx4 v71, v[92:95], s[58:59] offset:64
	v_mul_f32_e32 v36, v36, v67
	v_mul_f32_e32 v37, v37, v67
	v_mul_f32_e32 v38, v38, v67
	v_mul_f32_e32 v39, v39, v67
	v_mul_f32_e32 v44, v44, v67
	v_mul_f32_e32 v45, v45, v67
	v_mul_f32_e32 v46, v46, v67
	v_mul_f32_e32 v47, v47, v67
	v_cvt_pk_bf16_f32 v72, v36, v37
	v_cvt_pk_bf16_f32 v73, v38, v39
	v_cvt_pk_bf16_f32 v74, v44, v45
	v_cvt_pk_bf16_f32 v75, v46, v47
	s_nop 1
	v_permlane16_swap_b32_e32 v72, v74
	v_permlane16_swap_b32_e32 v73, v75
	s_nop 1
	global_store_dwordx4 v71, v[72:75], s[58:59] offset:128
	v_mul_f32_e32 v52, v52, v67
	v_mul_f32_e32 v53, v53, v67
	v_mul_f32_e32 v54, v54, v67
	v_mul_f32_e32 v55, v55, v67
	v_mul_f32_e32 v60, v60, v67
	v_mul_f32_e32 v61, v61, v67
	v_mul_f32_e32 v62, v62, v67
	v_mul_f32_e32 v63, v63, v67
	v_cvt_pk_bf16_f32 v76, v52, v53
	v_cvt_pk_bf16_f32 v77, v54, v55
	v_cvt_pk_bf16_f32 v78, v60, v61
	v_cvt_pk_bf16_f32 v79, v62, v63
	s_nop 1
	v_permlane16_swap_b32_e32 v76, v78
	v_permlane16_swap_b32_e32 v77, v79
	s_nop 1
	global_store_dwordx4 v71, v[76:79], s[58:59] offset:192
	s_barrier
